# expert GEMM1 unit loops: next unit's four token-index loads issued together and completed right before the K-loop instead of four load+wait round trips (on top of v56)
# baseline (speedup 1.0000x reference)
.LBB0_992:
	s_mov_b32 s98, 0
	s_add_i32 s53, s53, 1
	s_mul_i32 s2, s53, s60
	s_mul_hi_u32 s3, s53, s91
	s_add_i32 s3, s3, s2
	s_mul_i32 s2, s53, s91
	s_add_u32 s8, s2, s96
	s_addc_u32 s9, s3, s97
	v_cmp_ge_i64_e32 vcc, s[8:9], v[136:137]
	v_cmp_lt_i64_e64 s[10:11], s[8:9], v[136:137]
	s_cbranch_vccnz .LBB0_994
	s_ashr_i32 s2, s9, 31
	s_lshr_b32 s2, s2, 30
	s_add_u32 s2, s8, s2
	s_addc_u32 s3, s9, 0
	s_lshr_b64 s[28:29], s[2:3], 2
	s_add_i32 s2, s28, 0
	s_add_i32 s2, s2, 0x24e00
	v_mov_b32_e32 v2, s2
	ds_read_u8 v2, v2
	s_lshl_b32 s2, s28, 2
	s_sub_i32 s29, s8, s2
	s_waitcnt lgkmcnt(0)
	v_readfirstlane_b32 s2, v2
	s_lshl_b32 s2, s2, 2
	s_add_i32 s30, s2, s29
.LBB0_994:
	s_nop 0
	v_cndmask_b32_e64 v2, 0, 1, s[10:11]
	v_cmp_ne_u32_e64 s[8:9], 1, v2
	s_andn2_b64 vcc, exec, s[10:11]
	v_mov_b32_e32 v162, v142
	v_mov_b32_e32 v161, v138
	v_mov_b32_e32 v163, v140
	v_mov_b32_e32 v164, v148
	s_cbranch_vccnz .LBB0_1004
	s_add_i32 s2, s28, 0
	s_add_i32 s2, s2, 0x24e00
	v_mov_b32_e32 v2, s2
	ds_read_u8 v2, v2
	v_mov_b32_e32 v6, 0
	v_mov_b32_e32 v7, 0
	s_waitcnt lgkmcnt(0)
	v_readfirstlane_b32 s2, v2
	s_lshl_b32 s3, s2, 2
	s_add_i32 s3, s3, 0
	s_add_i32 s31, s3, 0x24d00
	s_add_i32 s3, s3, 0x25000
	v_mov_b32_e32 v2, s31
	v_mov_b32_e32 v3, s3
	ds_read_b32 v2, v2
	ds_read_b32 v3, v3
	s_ashr_i32 s3, s2, 31
	s_lshl_b32 s31, s28, 8
	s_lshl_b64 s[34:35], s[2:3], 17
	s_waitcnt lgkmcnt(0)
	v_readfirstlane_b32 s3, v2
	s_sub_i32 s3, s31, s3
	v_readfirstlane_b32 s2, v3
	s_add_u32 s34, s4, s34
	v_add_u32_e32 v2, s3, v1
	s_addc_u32 s35, s5, s35
	v_cmp_gt_i32_e32 vcc, s2, v2
	v_ashrrev_i32_e32 v3, 31, v2
	v_mov_b32_e32 v164, 0
	v_mov_b32_e32 v163, 0
	v_mov_b32_e32 v161, 0
	v_mov_b32_e32 v162, 0
	v_lshl_add_u64 v[10:11], v[2:3], 2, s[34:35]
	v_add_u32_e32 v4, s3, v149
	v_ashrrev_i32_e32 v5, 31, v4
	v_lshl_add_u64 v[12:13], v[4:5], 2, s[34:35]
	s_and_saveexec_b64 s[40:41], vcc
	global_load_dword v164, v[10:11], off
	s_or_b64 exec, exec, s[40:41]
	v_cmp_gt_i32_e32 vcc, s2, v4
	s_nop 1
	s_and_saveexec_b64 s[40:41], vcc
	global_load_dword v163, v[12:13], off
	s_or_b64 exec, exec, s[40:41]
	s_addk_i32 s3, 0x80
	v_add_u32_e32 v8, s3, v1
	v_cmp_gt_i32_e32 vcc, s2, v8
	s_nop 1
	s_and_saveexec_b64 s[40:41], vcc
	global_load_dword v161, v[10:11], off offset:512
	s_or_b64 exec, exec, s[40:41]
	v_add_u32_e32 v8, s3, v149
	v_cmp_gt_i32_e32 vcc, s2, v8
	s_nop 1
	s_and_saveexec_b64 s[40:41], vcc
	global_load_dword v162, v[12:13], off offset:512
	s_or_b64 exec, exec, s[40:41]
	s_mov_b32 s98, 1
.LBB0_1004:
	s_ashr_i32 s31, s30, 31
	s_lshl_b64 s[2:3], s[30:31], 20
	s_add_u32 s34, s42, s2
	s_addc_u32 s35, s43, s3
	s_and_b64 s[2:3], s[10:11], exec
	s_cselect_b32 s31, s35, s39
	s_cselect_b32 s37, s34, s38
	v_mov_b32_e32 v139, v131
	v_mov_b32_e32 v143, v131
	s_add_u32 s64, s38, 0x100
	v_mov_b32_e32 v2, 0
	s_addc_u32 s65, s39, 0
	v_lshl_add_u64 v[144:145], s[22:23], 0, v[142:143]
	v_lshl_add_u64 v[146:147], s[22:23], 0, v[138:139]
	s_mov_b32 s66, -2
	s_mov_b64 s[10:11], 0
	v_mov_b32_e32 v3, v2
	v_mov_b32_e32 v4, v2
	v_mov_b32_e32 v5, v2
	v_mov_b32_e32 v6, v2
	v_mov_b32_e32 v7, v2
	v_mov_b32_e32 v8, v2
	v_mov_b32_e32 v9, v2
	v_mov_b32_e32 v18, v2
	v_mov_b32_e32 v19, v2
	v_mov_b32_e32 v20, v2
	v_mov_b32_e32 v21, v2
	v_mov_b32_e32 v22, v2
	v_mov_b32_e32 v23, v2
	v_mov_b32_e32 v24, v2
	v_mov_b32_e32 v25, v2
	v_mov_b32_e32 v34, v2
	v_mov_b32_e32 v35, v2
	v_mov_b32_e32 v36, v2
	v_mov_b32_e32 v37, v2
	v_mov_b32_e32 v38, v2
	v_mov_b32_e32 v39, v2
	v_mov_b32_e32 v40, v2
	v_mov_b32_e32 v41, v2
	v_mov_b32_e32 v50, v2
	v_mov_b32_e32 v51, v2
	v_mov_b32_e32 v52, v2
	v_mov_b32_e32 v53, v2
	v_mov_b32_e32 v54, v2
	v_mov_b32_e32 v55, v2
	v_mov_b32_e32 v56, v2
	v_mov_b32_e32 v57, v2
	v_mov_b32_e32 v10, v2
	v_mov_b32_e32 v11, v2
	v_mov_b32_e32 v12, v2
	v_mov_b32_e32 v13, v2
	v_mov_b32_e32 v14, v2
	v_mov_b32_e32 v15, v2
	v_mov_b32_e32 v16, v2
	v_mov_b32_e32 v17, v2
	v_mov_b32_e32 v26, v2
	v_mov_b32_e32 v27, v2
	v_mov_b32_e32 v28, v2
	v_mov_b32_e32 v29, v2
	v_mov_b32_e32 v30, v2
	v_mov_b32_e32 v31, v2
	v_mov_b32_e32 v32, v2
	v_mov_b32_e32 v33, v2
	v_mov_b32_e32 v42, v2
	v_mov_b32_e32 v43, v2
	v_mov_b32_e32 v44, v2
	v_mov_b32_e32 v45, v2
	v_mov_b32_e32 v46, v2
	v_mov_b32_e32 v47, v2
	v_mov_b32_e32 v48, v2
	v_mov_b32_e32 v49, v2
	v_mov_b32_e32 v58, v2
	v_mov_b32_e32 v59, v2
	v_mov_b32_e32 v60, v2
	v_mov_b32_e32 v61, v2
	v_mov_b32_e32 v62, v2
	v_mov_b32_e32 v63, v2
	v_mov_b32_e32 v64, v2
	v_mov_b32_e32 v65, v2
	v_mov_b32_e32 v66, v2
	v_mov_b32_e32 v67, v2
	v_mov_b32_e32 v68, v2
	v_mov_b32_e32 v69, v2
	v_mov_b32_e32 v70, v2
	v_mov_b32_e32 v71, v2
	v_mov_b32_e32 v72, v2
	v_mov_b32_e32 v73, v2
	v_mov_b32_e32 v82, v2
	v_mov_b32_e32 v83, v2
	v_mov_b32_e32 v84, v2
	v_mov_b32_e32 v85, v2
	v_mov_b32_e32 v86, v2
	v_mov_b32_e32 v87, v2
	v_mov_b32_e32 v88, v2
	v_mov_b32_e32 v89, v2
	v_mov_b32_e32 v98, v2
	v_mov_b32_e32 v99, v2
	v_mov_b32_e32 v100, v2
	v_mov_b32_e32 v101, v2
	v_mov_b32_e32 v102, v2
	v_mov_b32_e32 v103, v2
	v_mov_b32_e32 v104, v2
	v_mov_b32_e32 v105, v2
	v_mov_b32_e32 v114, v2
	v_mov_b32_e32 v115, v2
	v_mov_b32_e32 v116, v2
	v_mov_b32_e32 v117, v2
	v_mov_b32_e32 v118, v2
	v_mov_b32_e32 v119, v2
	v_mov_b32_e32 v120, v2
	v_mov_b32_e32 v121, v2
	v_mov_b32_e32 v74, v2
	v_mov_b32_e32 v75, v2
	v_mov_b32_e32 v76, v2
	v_mov_b32_e32 v77, v2
	v_mov_b32_e32 v78, v2
	v_mov_b32_e32 v79, v2
	v_mov_b32_e32 v80, v2
	v_mov_b32_e32 v81, v2
	v_mov_b32_e32 v90, v2
	v_mov_b32_e32 v91, v2
	v_mov_b32_e32 v92, v2
	v_mov_b32_e32 v93, v2
	v_mov_b32_e32 v94, v2
	v_mov_b32_e32 v95, v2
	v_mov_b32_e32 v96, v2
	v_mov_b32_e32 v97, v2
	v_mov_b32_e32 v106, v2
	v_mov_b32_e32 v107, v2
	v_mov_b32_e32 v108, v2
	v_mov_b32_e32 v109, v2
	v_mov_b32_e32 v110, v2
	v_mov_b32_e32 v111, v2
	v_mov_b32_e32 v112, v2
	v_mov_b32_e32 v113, v2
	v_mov_b32_e32 v122, v2
	v_mov_b32_e32 v123, v2
	v_mov_b32_e32 v124, v2
	v_mov_b32_e32 v125, v2
	v_mov_b32_e32 v126, v2
	v_mov_b32_e32 v127, v2
	v_mov_b32_e32 v128, v2
	v_mov_b32_e32 v129, v2
	s_cmp_eq_u32 s98, 0
	s_cbranch_scc1 .Lmoe_ix_ready_0
	s_waitcnt vmcnt(0)
	v_lshlrev_b32_e32 v161, 12, v161
	v_lshlrev_b32_e32 v163, 12, v163
	v_lshlrev_b32_e32 v164, 12, v164
	v_lshlrev_b32_e32 v162, 12, v162
	v_or_b32_e32 v161, v161, v151
	v_or_b32_e32 v163, v163, v151
	v_or_b32_e32 v164, v164, v151
	v_or_b32_e32 v162, v162, v151
.Lmoe_ix_ready_0:
.LBB0_1005:
	ds_read_b128 v[152:155], v158
	ds_read_b128 v[166:169], v158 offset:1024
	ds_read_b128 v[170:173], v158 offset:2048
	ds_read_b128 v[174:177], v158 offset:3072
	ds_read_b128 v[178:181], v159
	ds_read_b128 v[182:185], v159 offset:1024
	ds_read_b128 v[186:189], v159 offset:2048
	ds_read_b128 v[190:193], v159 offset:3072
	s_add_u32 s40, s64, s10
	s_addc_u32 s41, s65, s11
	s_add_u32 s38, s10, 0x100
	s_addc_u32 s39, s11, 0
	s_cmpk_eq_i32 s10, 0xf00
	s_cselect_b64 vcc, -1, 0
	s_and_b64 s[2:3], vcc, exec
	s_cselect_b32 s41, s31, s41
	s_cselect_b32 s40, s37, s40
	s_cselect_b32 s67, 0, s38
	v_lshl_add_u64 v[226:227], v[146:147], 0, s[10:11]
	s_add_i32 m0, s49, 0xc000
	ds_read_b128 v[194:197], v160
	ds_read_b128 v[198:201], v160 offset:1024
	ds_read_b128 v[202:205], v160 offset:2048
	ds_read_b128 v[206:209], v160 offset:3072
	ds_read_b128 v[210:213], v160 offset:4096
	ds_read_b128 v[214:217], v160 offset:5120
	ds_read_b128 v[218:221], v160 offset:6144
	ds_read_b128 v[222:225], v160 offset:7168
	global_load_lds_dwordx4 v[226:227], off
	v_lshl_add_u64 v[226:227], v[144:145], 0, s[10:11]
	s_add_i32 m0, s49, 0xe000
	s_nop 0
	global_load_lds_dwordx4 v[226:227], off
	s_waitcnt vmcnt(8)
	s_waitcnt lgkmcnt(0)
	s_barrier
	s_setprio 1
	s_waitcnt lgkmcnt(0)
	v_mfma_f32_16x16x32_bf16 v[126:129], v[152:155], v[194:197], v[126:129]
	v_mfma_f32_16x16x32_bf16 v[122:125], v[170:173], v[194:197], v[122:125]
	v_mfma_f32_16x16x32_bf16 v[110:113], v[152:155], v[202:205], v[110:113]
	v_mfma_f32_16x16x32_bf16 v[106:109], v[170:173], v[202:205], v[106:109]
	v_mfma_f32_16x16x32_bf16 v[94:97], v[152:155], v[210:213], v[94:97]
	v_mfma_f32_16x16x32_bf16 v[90:93], v[170:173], v[210:213], v[90:93]
	v_mfma_f32_16x16x32_bf16 v[78:81], v[152:155], v[218:221], v[78:81]
	v_mfma_f32_16x16x32_bf16 v[74:77], v[170:173], v[218:221], v[74:77]
	v_mfma_f32_16x16x32_bf16 v[126:129], v[166:169], v[198:201], v[126:129]
	v_mfma_f32_16x16x32_bf16 v[122:125], v[174:177], v[198:201], v[122:125]
	v_mfma_f32_16x16x32_bf16 v[110:113], v[166:169], v[206:209], v[110:113]
	v_mfma_f32_16x16x32_bf16 v[106:109], v[174:177], v[206:209], v[106:109]
	v_mfma_f32_16x16x32_bf16 v[94:97], v[166:169], v[214:217], v[94:97]
	v_mfma_f32_16x16x32_bf16 v[90:93], v[174:177], v[214:217], v[90:93]
	v_mfma_f32_16x16x32_bf16 v[78:81], v[166:169], v[222:225], v[78:81]
	v_mfma_f32_16x16x32_bf16 v[74:77], v[174:177], v[222:225], v[74:77]
	s_setprio 0
	s_setprio 1
	v_mfma_f32_16x16x32_bf16 v[118:121], v[178:181], v[194:197], v[118:121]
	v_mfma_f32_16x16x32_bf16 v[114:117], v[186:189], v[194:197], v[114:117]
	v_mfma_f32_16x16x32_bf16 v[102:105], v[178:181], v[202:205], v[102:105]
	v_mfma_f32_16x16x32_bf16 v[98:101], v[186:189], v[202:205], v[98:101]
	v_mfma_f32_16x16x32_bf16 v[86:89], v[178:181], v[210:213], v[86:89]
	v_mfma_f32_16x16x32_bf16 v[82:85], v[186:189], v[210:213], v[82:85]
	v_mfma_f32_16x16x32_bf16 v[70:73], v[178:181], v[218:221], v[70:73]
	v_mfma_f32_16x16x32_bf16 v[66:69], v[186:189], v[218:221], v[66:69]
	v_mfma_f32_16x16x32_bf16 v[118:121], v[182:185], v[198:201], v[118:121]
	v_mfma_f32_16x16x32_bf16 v[114:117], v[190:193], v[198:201], v[114:117]
	v_mfma_f32_16x16x32_bf16 v[102:105], v[182:185], v[206:209], v[102:105]
	v_mfma_f32_16x16x32_bf16 v[98:101], v[190:193], v[206:209], v[98:101]
	v_mfma_f32_16x16x32_bf16 v[86:89], v[182:185], v[214:217], v[86:89]
	v_mfma_f32_16x16x32_bf16 v[82:85], v[190:193], v[214:217], v[82:85]
	v_mfma_f32_16x16x32_bf16 v[70:73], v[182:185], v[222:225], v[70:73]
	v_mfma_f32_16x16x32_bf16 v[66:69], v[190:193], v[222:225], v[66:69]
	s_setprio 0
	s_barrier
	s_add_i32 s2, s61, s48
	v_lshl_add_u64 v[226:227], s[40:41], 0, v[132:133]
	s_mov_b32 m0, s2
	ds_read_b128 v[194:197], v160 offset:16384
	ds_read_b128 v[198:201], v160 offset:17408
	ds_read_b128 v[202:205], v160 offset:18432
	ds_read_b128 v[206:209], v160 offset:19456
	ds_read_b128 v[210:213], v160 offset:20480
	ds_read_b128 v[214:217], v160 offset:21504
	ds_read_b128 v[218:221], v160 offset:22528
	ds_read_b128 v[222:225], v160 offset:23552
	global_load_lds_dwordx4 v[226:227], off
	s_add_i32 m0, s2, 0x2000
	s_add_u32 s2, s40, 0x80000
	v_lshl_add_u64 v[228:229], s[40:41], 0, v[134:135]
	s_addc_u32 s3, s41, 0
	s_add_i32 s10, s62, s48
	global_load_lds_dwordx4 v[228:229], off
	v_lshl_add_u64 v[230:231], s[2:3], 0, v[132:133]
	s_mov_b32 m0, s10
	v_cndmask_b32_e32 v130, v148, v164, vcc
	global_load_lds_dwordx4 v[230:231], off
	s_add_i32 m0, s10, 0x2000
	v_lshl_add_u64 v[230:231], s[2:3], 0, v[134:135]
	s_add_u32 s2, s16, s67
	global_load_lds_dwordx4 v[230:231], off
	s_addc_u32 s3, s17, 0
	s_mov_b32 m0, s49
	v_lshl_add_u64 v[230:231], s[2:3], 0, v[130:131]
	global_load_lds_dwordx4 v130, s[2:3]
	v_cndmask_b32_e32 v130, v140, v163, vcc
	s_mov_b32 m0, s50
	v_lshl_add_u64 v[232:233], s[2:3], 0, v[130:131]
	global_load_lds_dwordx4 v130, s[2:3]
	s_waitcnt vmcnt(8)
	s_waitcnt lgkmcnt(0)
	s_barrier
	s_setprio 1
	s_waitcnt lgkmcnt(0)
	v_mfma_f32_16x16x32_bf16 v[62:65], v[152:155], v[194:197], v[62:65]
	v_mfma_f32_16x16x32_bf16 v[58:61], v[170:173], v[194:197], v[58:61]
	v_mfma_f32_16x16x32_bf16 v[46:49], v[152:155], v[202:205], v[46:49]
	v_mfma_f32_16x16x32_bf16 v[42:45], v[170:173], v[202:205], v[42:45]
	v_mfma_f32_16x16x32_bf16 v[30:33], v[152:155], v[210:213], v[30:33]
	v_mfma_f32_16x16x32_bf16 v[26:29], v[170:173], v[210:213], v[26:29]
	v_mfma_f32_16x16x32_bf16 v[14:17], v[152:155], v[218:221], v[14:17]
	v_mfma_f32_16x16x32_bf16 v[10:13], v[170:173], v[218:221], v[10:13]
	v_mfma_f32_16x16x32_bf16 v[62:65], v[166:169], v[198:201], v[62:65]
	v_mfma_f32_16x16x32_bf16 v[58:61], v[174:177], v[198:201], v[58:61]
	v_mfma_f32_16x16x32_bf16 v[46:49], v[166:169], v[206:209], v[46:49]
	v_mfma_f32_16x16x32_bf16 v[42:45], v[174:177], v[206:209], v[42:45]
	v_mfma_f32_16x16x32_bf16 v[30:33], v[166:169], v[214:217], v[30:33]
	v_mfma_f32_16x16x32_bf16 v[26:29], v[174:177], v[214:217], v[26:29]
	v_mfma_f32_16x16x32_bf16 v[14:17], v[166:169], v[222:225], v[14:17]
	v_mfma_f32_16x16x32_bf16 v[10:13], v[174:177], v[222:225], v[10:13]
	s_setprio 0
	s_setprio 1
	v_mfma_f32_16x16x32_bf16 v[54:57], v[178:181], v[194:197], v[54:57]
	v_mfma_f32_16x16x32_bf16 v[50:53], v[186:189], v[194:197], v[50:53]
	v_mfma_f32_16x16x32_bf16 v[38:41], v[178:181], v[202:205], v[38:41]
	v_mfma_f32_16x16x32_bf16 v[34:37], v[186:189], v[202:205], v[34:37]
	v_mfma_f32_16x16x32_bf16 v[22:25], v[178:181], v[210:213], v[22:25]
	v_mfma_f32_16x16x32_bf16 v[18:21], v[186:189], v[210:213], v[18:21]
	v_mfma_f32_16x16x32_bf16 v[6:9], v[178:181], v[218:221], v[6:9]
	v_mfma_f32_16x16x32_bf16 v[2:5], v[186:189], v[218:221], v[2:5]
	v_mfma_f32_16x16x32_bf16 v[54:57], v[182:185], v[198:201], v[54:57]
	v_mfma_f32_16x16x32_bf16 v[50:53], v[190:193], v[198:201], v[50:53]
	v_mfma_f32_16x16x32_bf16 v[38:41], v[182:185], v[206:209], v[38:41]
	v_mfma_f32_16x16x32_bf16 v[34:37], v[190:193], v[206:209], v[34:37]
	v_mfma_f32_16x16x32_bf16 v[22:25], v[182:185], v[214:217], v[22:25]
	v_mfma_f32_16x16x32_bf16 v[18:21], v[190:193], v[214:217], v[18:21]
	v_mfma_f32_16x16x32_bf16 v[6:9], v[182:185], v[222:225], v[6:9]
	v_mfma_f32_16x16x32_bf16 v[2:5], v[190:193], v[222:225], v[2:5]
	s_setprio 0
	s_barrier
	s_add_i32 s10, 0, 0x18000
	v_add_u32_e32 v130, s10, v156
	s_add_i32 s11, 0, 0x1c000
	ds_read_b128 v[152:155], v130
	ds_read_b128 v[166:169], v130 offset:1024
	ds_read_b128 v[170:173], v130 offset:2048
	ds_read_b128 v[174:177], v130 offset:3072
	v_add_u32_e32 v130, s11, v156
	ds_read_b128 v[178:181], v130
	ds_read_b128 v[182:185], v130 offset:1024
	ds_read_b128 v[186:189], v130 offset:2048
	ds_read_b128 v[190:193], v130 offset:3072
	s_mov_b32 m0, s51
	v_cndmask_b32_e32 v130, v138, v161, vcc
	ds_read_b128 v[194:197], v160 offset:32768
	ds_read_b128 v[198:201], v160 offset:33792
	ds_read_b128 v[202:205], v160 offset:34816
	ds_read_b128 v[206:209], v160 offset:35840
	ds_read_b128 v[210:213], v160 offset:36864
	ds_read_b128 v[214:217], v160 offset:37888
	ds_read_b128 v[218:221], v160 offset:38912
	ds_read_b128 v[222:225], v160 offset:39936
	global_load_lds_dwordx4 v130, s[2:3]
	v_cndmask_b32_e32 v130, v142, v162, vcc
	s_mov_b32 m0, s52
	s_nop 0
	global_load_lds_dwordx4 v130, s[2:3]
	s_waitcnt vmcnt(8)
	s_waitcnt lgkmcnt(0)
	s_barrier
	s_setprio 1
	s_waitcnt lgkmcnt(0)
	v_mfma_f32_16x16x32_bf16 v[126:129], v[152:155], v[194:197], v[126:129]
	v_mfma_f32_16x16x32_bf16 v[122:125], v[170:173], v[194:197], v[122:125]
	v_mfma_f32_16x16x32_bf16 v[110:113], v[152:155], v[202:205], v[110:113]
	v_mfma_f32_16x16x32_bf16 v[106:109], v[170:173], v[202:205], v[106:109]
	v_mfma_f32_16x16x32_bf16 v[94:97], v[152:155], v[210:213], v[94:97]
	v_mfma_f32_16x16x32_bf16 v[90:93], v[170:173], v[210:213], v[90:93]
	v_mfma_f32_16x16x32_bf16 v[78:81], v[152:155], v[218:221], v[78:81]
	v_mfma_f32_16x16x32_bf16 v[74:77], v[170:173], v[218:221], v[74:77]
	v_mfma_f32_16x16x32_bf16 v[126:129], v[166:169], v[198:201], v[126:129]
	v_mfma_f32_16x16x32_bf16 v[122:125], v[174:177], v[198:201], v[122:125]
	v_mfma_f32_16x16x32_bf16 v[110:113], v[166:169], v[206:209], v[110:113]
	v_mfma_f32_16x16x32_bf16 v[106:109], v[174:177], v[206:209], v[106:109]
	v_mfma_f32_16x16x32_bf16 v[94:97], v[166:169], v[214:217], v[94:97]
	v_mfma_f32_16x16x32_bf16 v[90:93], v[174:177], v[214:217], v[90:93]
	v_mfma_f32_16x16x32_bf16 v[78:81], v[166:169], v[222:225], v[78:81]
	v_mfma_f32_16x16x32_bf16 v[74:77], v[174:177], v[222:225], v[74:77]
	s_setprio 0
	s_setprio 1
	v_mfma_f32_16x16x32_bf16 v[118:121], v[178:181], v[194:197], v[118:121]
	v_mfma_f32_16x16x32_bf16 v[114:117], v[186:189], v[194:197], v[114:117]
	v_mfma_f32_16x16x32_bf16 v[102:105], v[178:181], v[202:205], v[102:105]
	v_mfma_f32_16x16x32_bf16 v[98:101], v[186:189], v[202:205], v[98:101]
	v_mfma_f32_16x16x32_bf16 v[86:89], v[178:181], v[210:213], v[86:89]
	v_mfma_f32_16x16x32_bf16 v[82:85], v[186:189], v[210:213], v[82:85]
	v_mfma_f32_16x16x32_bf16 v[70:73], v[178:181], v[218:221], v[70:73]
	v_mfma_f32_16x16x32_bf16 v[66:69], v[186:189], v[218:221], v[66:69]
	v_mfma_f32_16x16x32_bf16 v[118:121], v[182:185], v[198:201], v[118:121]
	v_mfma_f32_16x16x32_bf16 v[114:117], v[190:193], v[198:201], v[114:117]
	v_mfma_f32_16x16x32_bf16 v[102:105], v[182:185], v[206:209], v[102:105]
	v_mfma_f32_16x16x32_bf16 v[98:101], v[190:193], v[206:209], v[98:101]
	v_mfma_f32_16x16x32_bf16 v[86:89], v[182:185], v[214:217], v[86:89]
	v_mfma_f32_16x16x32_bf16 v[82:85], v[190:193], v[214:217], v[82:85]
	v_mfma_f32_16x16x32_bf16 v[70:73], v[182:185], v[222:225], v[70:73]
	v_mfma_f32_16x16x32_bf16 v[66:69], v[190:193], v[222:225], v[66:69]
	s_setprio 0
	s_barrier
	s_add_i32 s2, s10, s48
	v_lshl_add_u64 v[226:227], v[226:227], 0, s[20:21]
	s_mov_b32 m0, s2
	ds_read_b128 v[194:197], v160 offset:49152
	ds_read_b128 v[198:201], v160 offset:50176
	ds_read_b128 v[202:205], v160 offset:51200
	ds_read_b128 v[206:209], v160 offset:52224
	ds_read_b128 v[210:213], v160 offset:53248
	ds_read_b128 v[214:217], v160 offset:54272
	ds_read_b128 v[218:221], v160 offset:55296
	ds_read_b128 v[222:225], v160 offset:56320
	global_load_lds_dwordx4 v[226:227], off
	s_add_i32 m0, s2, 0x2000
	s_add_u32 s2, s40, 0x80080
	v_lshl_add_u64 v[226:227], v[228:229], 0, s[20:21]
	s_addc_u32 s3, s41, 0
	s_add_i32 s10, s11, s48
	global_load_lds_dwordx4 v[226:227], off
	v_lshl_add_u64 v[226:227], s[2:3], 0, v[132:133]
	s_mov_b32 m0, s10
	s_nop 0
	global_load_lds_dwordx4 v[226:227], off
	v_lshl_add_u64 v[226:227], s[2:3], 0, v[134:135]
	s_add_i32 m0, s10, 0x2000
	s_nop 0
	global_load_lds_dwordx4 v[226:227], off
	v_lshl_add_u64 v[226:227], v[230:231], 0, s[20:21]
	s_mov_b32 m0, s58
	s_nop 0
	global_load_lds_dwordx4 v[226:227], off
	v_lshl_add_u64 v[226:227], v[232:233], 0, s[20:21]
	s_mov_b32 m0, s59
	s_nop 0
	global_load_lds_dwordx4 v[226:227], off
	s_waitcnt vmcnt(8)
	s_waitcnt lgkmcnt(0)
	s_barrier
	s_setprio 1
	s_waitcnt lgkmcnt(0)
	v_mfma_f32_16x16x32_bf16 v[62:65], v[152:155], v[194:197], v[62:65]
	v_mfma_f32_16x16x32_bf16 v[58:61], v[170:173], v[194:197], v[58:61]
	v_mfma_f32_16x16x32_bf16 v[46:49], v[152:155], v[202:205], v[46:49]
	v_mfma_f32_16x16x32_bf16 v[42:45], v[170:173], v[202:205], v[42:45]
	v_mfma_f32_16x16x32_bf16 v[30:33], v[152:155], v[210:213], v[30:33]
	v_mfma_f32_16x16x32_bf16 v[26:29], v[170:173], v[210:213], v[26:29]
	v_mfma_f32_16x16x32_bf16 v[14:17], v[152:155], v[218:221], v[14:17]
	v_mfma_f32_16x16x32_bf16 v[10:13], v[170:173], v[218:221], v[10:13]
	v_mfma_f32_16x16x32_bf16 v[62:65], v[166:169], v[198:201], v[62:65]
	v_mfma_f32_16x16x32_bf16 v[58:61], v[174:177], v[198:201], v[58:61]
	v_mfma_f32_16x16x32_bf16 v[46:49], v[166:169], v[206:209], v[46:49]
	v_mfma_f32_16x16x32_bf16 v[42:45], v[174:177], v[206:209], v[42:45]
	v_mfma_f32_16x16x32_bf16 v[30:33], v[166:169], v[214:217], v[30:33]
	v_mfma_f32_16x16x32_bf16 v[26:29], v[174:177], v[214:217], v[26:29]
	v_mfma_f32_16x16x32_bf16 v[14:17], v[166:169], v[222:225], v[14:17]
	v_mfma_f32_16x16x32_bf16 v[10:13], v[174:177], v[222:225], v[10:13]
	s_setprio 0
	s_setprio 1
	v_mfma_f32_16x16x32_bf16 v[54:57], v[178:181], v[194:197], v[54:57]
	v_mfma_f32_16x16x32_bf16 v[50:53], v[186:189], v[194:197], v[50:53]
	v_mfma_f32_16x16x32_bf16 v[38:41], v[178:181], v[202:205], v[38:41]
	v_mfma_f32_16x16x32_bf16 v[34:37], v[186:189], v[202:205], v[34:37]
	v_mfma_f32_16x16x32_bf16 v[22:25], v[178:181], v[210:213], v[22:25]
	v_mfma_f32_16x16x32_bf16 v[18:21], v[186:189], v[210:213], v[18:21]
	v_mfma_f32_16x16x32_bf16 v[6:9], v[178:181], v[218:221], v[6:9]
	v_mfma_f32_16x16x32_bf16 v[2:5], v[186:189], v[218:221], v[2:5]
	v_mfma_f32_16x16x32_bf16 v[54:57], v[182:185], v[198:201], v[54:57]
	v_mfma_f32_16x16x32_bf16 v[50:53], v[190:193], v[198:201], v[50:53]
	v_mfma_f32_16x16x32_bf16 v[38:41], v[182:185], v[206:209], v[38:41]
	v_mfma_f32_16x16x32_bf16 v[34:37], v[190:193], v[206:209], v[34:37]
	v_mfma_f32_16x16x32_bf16 v[22:25], v[182:185], v[214:217], v[22:25]
	v_mfma_f32_16x16x32_bf16 v[18:21], v[190:193], v[214:217], v[18:21]
	v_mfma_f32_16x16x32_bf16 v[6:9], v[182:185], v[222:225], v[6:9]
	v_mfma_f32_16x16x32_bf16 v[2:5], v[190:193], v[222:225], v[2:5]
	s_setprio 0
	s_barrier
	s_add_i32 s66, s66, 2
	s_cmp_gt_u32 s66, 29
	s_mov_b64 s[10:11], s[38:39]
	s_cbranch_scc0 .LBB0_1005
	s_and_b64 vcc, exec, s[24:25]
	s_cbranch_vccz .LBB0_1008
	s_barrier
